# cache policy: nt on the prologue's read-once f32 weight / input loads
# speedup vs baseline: 1.0012x; 1.0012x over previous
.LBB0_19:
	s_cmpk_gt_i32 s88, 0x2bff
	s_mov_b64 s[4:5], -1
	s_cbranch_scc0 .LBB0_139
	s_cmpk_gt_u32 s88, 0x41ff
	s_cbranch_scc0 .LBB0_136
	s_cmpk_gt_u32 s88, 0x62ff
	s_cbranch_scc0 .LBB0_27
	s_cmpk_gt_u32 s88, 0x66ff
	s_cbranch_scc0 .LBB0_24
	s_add_i32 s4, s88, 0xffff9900
	s_lshr_b32 s30, s4, 7
	s_lshl_b64 s[4:5], s[30:31], 20
	s_add_u32 s4, s16, s4
	s_addc_u32 s5, s17, s5
	s_lshl_b64 s[38:39], s[30:31], 19
	s_add_u32 s38, s47, s38
	s_addc_u32 s39, s48, s39
	s_lshl_b32 s30, s88, 1
	s_and_b32 s40, s30, 0xc0
	s_lshl_b32 s30, s88, 5
	s_and_b32 s30, s30, 0x3e0
	v_or_b32_e32 v6, s40, v2
	v_lshl_or_b32 v6, v6, 10, s30
	v_or_b32_e32 v8, v6, v40
	v_or_b32_e32 v9, v6, v5
	v_or_b32_e32 v10, v6, v30
	v_or_b32_e32 v11, v6, v31
	v_or_b32_e32 v12, v6, v32
	v_or_b32_e32 v13, v6, v33
	v_or_b32_e32 v14, v6, v34
	v_or_b32_e32 v15, v6, v35
	v_or_b32_e32 v16, v6, v36
	v_or_b32_e32 v17, v6, v37
	v_or_b32_e32 v18, v6, v38
	v_or_b32_e32 v19, v6, v39
	v_or_b32_e32 v20, v6, v41
	v_or_b32_e32 v21, v6, v42
	v_or_b32_e32 v22, v6, v43
	v_or_b32_e32 v23, v6, v44
	v_lshlrev_b32_e32 v8, 2, v8
	v_lshlrev_b32_e32 v9, 2, v9
	v_lshlrev_b32_e32 v10, 2, v10
	v_lshlrev_b32_e32 v11, 2, v11
	v_lshlrev_b32_e32 v12, 2, v12
	v_lshlrev_b32_e32 v13, 2, v13
	v_lshlrev_b32_e32 v14, 2, v14
	v_lshlrev_b32_e32 v15, 2, v15
	v_lshlrev_b32_e32 v16, 2, v16
	v_lshlrev_b32_e32 v17, 2, v17
	v_lshlrev_b32_e32 v18, 2, v18
	v_lshlrev_b32_e32 v19, 2, v19
	v_lshlrev_b32_e32 v20, 2, v20
	v_lshlrev_b32_e32 v21, 2, v21
	v_lshlrev_b32_e32 v22, 2, v22
	v_lshlrev_b32_e32 v23, 2, v23
	global_load_dword v8, v8, s[4:5] nt
	s_nop 0
	global_load_dword v9, v9, s[4:5] nt
	s_nop 0
	global_load_dword v10, v10, s[4:5] nt
	s_nop 0
	global_load_dword v11, v11, s[4:5] nt
	s_nop 0
	global_load_dword v12, v12, s[4:5] nt
	s_nop 0
	global_load_dword v13, v13, s[4:5] nt
	s_nop 0
	global_load_dword v14, v14, s[4:5] nt
	s_nop 0
	global_load_dword v15, v15, s[4:5] nt
	s_nop 0
	global_load_dword v16, v16, s[4:5] nt
	s_nop 0
	global_load_dword v17, v17, s[4:5] nt
	s_nop 0
	global_load_dword v18, v18, s[4:5] nt
	s_nop 0
	global_load_dword v19, v19, s[4:5] nt
	s_nop 0
	global_load_dword v20, v20, s[4:5] nt
	s_nop 0
	global_load_dword v21, v21, s[4:5] nt
	s_nop 0
	global_load_dword v22, v22, s[4:5] nt
	s_nop 0
	global_load_dword v23, v23, s[4:5] nt
	v_or_b32_e32 v24, v6, v45
	v_or_b32_e32 v25, v6, v46
	v_or_b32_e32 v26, v6, v47
	v_or_b32_e32 v27, v6, v48
	v_or_b32_e32 v28, v6, v49
	v_or_b32_e32 v29, v6, v50
	v_or_b32_e32 v82, v6, v51
	v_or_b32_e32 v83, v6, v52
	v_lshlrev_b32_e32 v24, 2, v24
	v_lshlrev_b32_e32 v25, 2, v25
	v_lshlrev_b32_e32 v26, 2, v26
	v_lshlrev_b32_e32 v27, 2, v27
	v_lshlrev_b32_e32 v28, 2, v28
	v_lshlrev_b32_e32 v29, 2, v29
	v_lshlrev_b32_e32 v82, 2, v82
	v_lshlrev_b32_e32 v83, 2, v83
	global_load_dword v24, v24, s[4:5] nt
	s_nop 0
	global_load_dword v25, v25, s[4:5] nt
	s_nop 0
	global_load_dword v26, v26, s[4:5] nt
	s_nop 0
	global_load_dword v27, v27, s[4:5] nt
	s_nop 0
	global_load_dword v28, v28, s[4:5] nt
	s_nop 0
	global_load_dword v29, v29, s[4:5] nt
	s_nop 0
	global_load_dword v82, v82, s[4:5] nt
	s_nop 0
	global_load_dword v83, v83, s[4:5] nt
	v_or_b32_e32 v84, v6, v53
	v_or_b32_e32 v85, v6, v54
	v_or_b32_e32 v86, v6, v55
	v_or_b32_e32 v87, v6, v56
	v_or_b32_e32 v88, v6, v57
	v_or_b32_e32 v89, v6, v58
	v_or_b32_e32 v90, v6, v59
	v_or_b32_e32 v6, v6, v60
	v_lshlrev_b32_e32 v84, 2, v84
	v_lshlrev_b32_e32 v85, 2, v85
	v_lshlrev_b32_e32 v86, 2, v86
	v_lshlrev_b32_e32 v87, 2, v87
	v_lshlrev_b32_e32 v88, 2, v88
	v_lshlrev_b32_e32 v89, 2, v89
	v_lshlrev_b32_e32 v90, 2, v90
	v_lshlrev_b32_e32 v6, 2, v6
	global_load_dword v84, v84, s[4:5] nt
	s_nop 0
	global_load_dword v85, v85, s[4:5] nt
	s_nop 0
	global_load_dword v86, v86, s[4:5] nt
	s_nop 0
	global_load_dword v87, v87, s[4:5] nt
	s_nop 0
	global_load_dword v88, v88, s[4:5] nt
	s_nop 0
	global_load_dword v89, v89, s[4:5] nt
	s_nop 0
	global_load_dword v90, v90, s[4:5] nt
	s_nop 0
	global_load_dword v6, v6, s[4:5] nt
	s_lshl_b32 s4, s40, 1
	s_add_u32 s4, s38, s4
	s_addc_u32 s5, s39, 0
	s_waitcnt vmcnt(30)
	ds_write2_b32 v62, v8, v9 offset1:66
	s_waitcnt vmcnt(28)
	ds_write2_b32 v62, v10, v11 offset0:132 offset1:198
	s_waitcnt vmcnt(26)
	ds_write2_b32 v76, v12, v13 offset0:8 offset1:74
	s_waitcnt vmcnt(24)
	ds_write2_b32 v76, v14, v15 offset0:140 offset1:206
	s_waitcnt vmcnt(22)
	ds_write2_b32 v77, v16, v17 offset0:16 offset1:82
	s_waitcnt vmcnt(20)
	ds_write2_b32 v77, v18, v19 offset0:148 offset1:214
	s_waitcnt vmcnt(18)
	ds_write2_b32 v81, v20, v21 offset0:24 offset1:90
	s_waitcnt vmcnt(16)
	ds_write2_b32 v81, v22, v23 offset0:156 offset1:222
	v_add_u32_e32 v8, 0x1000, v62
	s_waitcnt vmcnt(14)
	ds_write2_b32 v8, v24, v25 offset0:32 offset1:98
	s_waitcnt vmcnt(12)
	ds_write2_b32 v8, v26, v27 offset0:164 offset1:230
	v_add_u32_e32 v8, 0x1400, v62
	s_waitcnt vmcnt(10)
	ds_write2_b32 v8, v28, v29 offset0:40 offset1:106
	s_waitcnt vmcnt(8)
	ds_write2_b32 v8, v82, v83 offset0:172 offset1:238
	v_add_u32_e32 v8, 0x1800, v62
	s_waitcnt vmcnt(6)
	ds_write2_b32 v8, v84, v85 offset0:48 offset1:114
	s_waitcnt vmcnt(4)
	ds_write2_b32 v8, v86, v87 offset0:180 offset1:246
	v_add_u32_e32 v8, 0x1c00, v62
	s_waitcnt vmcnt(2)
	ds_write2_b32 v8, v88, v89 offset0:56 offset1:122
	s_waitcnt vmcnt(0)
	ds_write2_b32 v8, v90, v6 offset0:188 offset1:254
	s_waitcnt lgkmcnt(0)
	ds_read2_b32 v[12:13], v64 offset0:33 offset1:41
	ds_read2_b32 v[14:15], v64 offset1:8
	ds_read2_b32 v[16:17], v64 offset0:66 offset1:74
	ds_read2_b32 v[18:19], v64 offset0:99 offset1:107
	ds_read2_b32 v[20:21], v64 offset0:132 offset1:140
	ds_read2_b32 v[22:23], v64 offset0:165 offset1:173
	ds_read2_b32 v[24:25], v64 offset0:198 offset1:206
	ds_read2_b32 v[26:27], v64 offset0:231 offset1:239
	v_lshlrev_b32_e32 v6, 1, v4
	v_lshl_add_u64 v[28:29], s[4:5], 0, v[6:7]
	v_or_b32_e32 v6, s30, v63
	v_lshlrev_b32_e32 v6, 9, v6
	s_waitcnt lgkmcnt(6)
	v_cvt_pk_bf16_f32 v8, v14, v12
	s_waitcnt lgkmcnt(4)
	v_cvt_pk_bf16_f32 v9, v16, v18
	s_waitcnt lgkmcnt(2)
	v_cvt_pk_bf16_f32 v10, v20, v22
	s_waitcnt lgkmcnt(0)
	v_cvt_pk_bf16_f32 v11, v24, v26
	v_lshl_add_u64 v[82:83], v[28:29], 0, v[6:7]
	global_store_dwordx4 v[82:83], v[8:11], off
	v_or_b32_e32 v6, s30, v65
	v_lshlrev_b32_e32 v6, 9, v6
	v_cvt_pk_bf16_f32 v8, v15, v13
	v_cvt_pk_bf16_f32 v9, v17, v19
	v_cvt_pk_bf16_f32 v10, v21, v23
	v_cvt_pk_bf16_f32 v11, v25, v27
	ds_read2_b32 v[14:15], v64 offset0:49 offset1:57
	ds_read2_b32 v[16:17], v64 offset0:16 offset1:24
	ds_read2_b32 v[18:19], v64 offset0:82 offset1:90
	ds_read2_b32 v[20:21], v64 offset0:115 offset1:123
	ds_read2_b32 v[22:23], v64 offset0:148 offset1:156
	ds_read2_b32 v[24:25], v64 offset0:181 offset1:189
	ds_read2_b32 v[26:27], v64 offset0:214 offset1:222
	ds_read2_b32 v[82:83], v64 offset0:247 offset1:255
	v_lshl_add_u64 v[12:13], v[28:29], 0, v[6:7]
	v_or_b32_e32 v6, s30, v66
	v_lshlrev_b32_e32 v6, 9, v6
	global_store_dwordx4 v[12:13], v[8:11], off
	v_lshl_add_u64 v[12:13], v[28:29], 0, v[6:7]
	v_or_b32_e32 v6, s30, v67
	s_waitcnt lgkmcnt(6)
	v_cvt_pk_bf16_f32 v8, v16, v14
	s_waitcnt lgkmcnt(4)
	v_cvt_pk_bf16_f32 v9, v18, v20
	s_waitcnt lgkmcnt(2)
	v_cvt_pk_bf16_f32 v10, v22, v24
	s_waitcnt lgkmcnt(0)
	v_cvt_pk_bf16_f32 v11, v26, v82
	v_lshlrev_b32_e32 v6, 9, v6
	global_store_dwordx4 v[12:13], v[8:11], off
	v_lshl_add_u64 v[12:13], v[28:29], 0, v[6:7]
	s_mov_b64 s[4:5], 0
	v_cvt_pk_bf16_f32 v8, v17, v15
	v_cvt_pk_bf16_f32 v9, v19, v21
	v_cvt_pk_bf16_f32 v10, v23, v25
	v_cvt_pk_bf16_f32 v11, v27, v83
	global_store_dwordx4 v[12:13], v[8:11], off
	s_waitcnt lgkmcnt(0)
.LBB0_24:
	s_andn2_b64 vcc, exec, s[4:5]
	s_cbranch_vccnz .LBB0_26
	s_add_i32 s40, s88, 0xffff9d00
	s_lshr_b32 s30, s40, 9
	s_lshl_b64 s[4:5], s[30:31], 22
	s_add_u32 s4, s18, s4
	s_addc_u32 s5, s19, s5
	s_lshl_b64 s[38:39], s[30:31], 21
	s_add_u32 s38, s49, s38
	s_addc_u32 s39, s50, s39
	s_lshl_b32 s30, s40, 1
	s_and_b32 s41, s30, 0x3c0
	s_lshl_b32 s30, s40, 5
	s_and_b32 s30, s30, 0x3e0
	v_or_b32_e32 v6, s41, v2
	v_lshl_or_b32 v6, v6, 10, s30
	v_or_b32_e32 v8, v6, v40
	v_or_b32_e32 v9, v6, v5
	v_or_b32_e32 v10, v6, v30
	v_or_b32_e32 v11, v6, v31
	v_or_b32_e32 v12, v6, v32
	v_or_b32_e32 v13, v6, v33
	v_or_b32_e32 v14, v6, v34
	v_or_b32_e32 v15, v6, v35
	v_or_b32_e32 v16, v6, v36
	v_or_b32_e32 v17, v6, v37
	v_or_b32_e32 v18, v6, v38
	v_or_b32_e32 v19, v6, v39
	v_or_b32_e32 v20, v6, v41
	v_or_b32_e32 v21, v6, v42
	v_or_b32_e32 v22, v6, v43
	v_or_b32_e32 v23, v6, v44
	v_lshlrev_b32_e32 v8, 2, v8
	v_lshlrev_b32_e32 v9, 2, v9
	v_lshlrev_b32_e32 v10, 2, v10
	v_lshlrev_b32_e32 v11, 2, v11
	v_lshlrev_b32_e32 v12, 2, v12
	v_lshlrev_b32_e32 v13, 2, v13
	v_lshlrev_b32_e32 v14, 2, v14
	v_lshlrev_b32_e32 v15, 2, v15
	v_lshlrev_b32_e32 v16, 2, v16
	v_lshlrev_b32_e32 v17, 2, v17
	v_lshlrev_b32_e32 v18, 2, v18
	v_lshlrev_b32_e32 v19, 2, v19
	v_lshlrev_b32_e32 v20, 2, v20
	v_lshlrev_b32_e32 v21, 2, v21
	v_lshlrev_b32_e32 v22, 2, v22
	v_lshlrev_b32_e32 v23, 2, v23
	global_load_dword v8, v8, s[4:5] nt
	s_nop 0
	global_load_dword v9, v9, s[4:5] nt
	s_nop 0
	global_load_dword v10, v10, s[4:5] nt
	s_nop 0
	global_load_dword v11, v11, s[4:5] nt
	s_nop 0
	global_load_dword v12, v12, s[4:5] nt
	s_nop 0
	global_load_dword v13, v13, s[4:5] nt
	s_nop 0
	global_load_dword v14, v14, s[4:5] nt
	s_nop 0
	global_load_dword v15, v15, s[4:5] nt
	s_nop 0
	global_load_dword v16, v16, s[4:5] nt
	s_nop 0
	global_load_dword v17, v17, s[4:5] nt
	s_nop 0
	global_load_dword v18, v18, s[4:5] nt
	s_nop 0
	global_load_dword v19, v19, s[4:5] nt
	s_nop 0
	global_load_dword v20, v20, s[4:5] nt
	s_nop 0
	global_load_dword v21, v21, s[4:5] nt
	s_nop 0
	global_load_dword v22, v22, s[4:5] nt
	s_nop 0
	global_load_dword v23, v23, s[4:5] nt
	v_or_b32_e32 v24, v6, v45
	v_or_b32_e32 v25, v6, v46
	v_or_b32_e32 v26, v6, v47
	v_or_b32_e32 v27, v6, v48
	v_or_b32_e32 v28, v6, v49
	v_or_b32_e32 v29, v6, v50
	v_or_b32_e32 v82, v6, v51
	v_or_b32_e32 v83, v6, v52
	v_lshlrev_b32_e32 v24, 2, v24
	v_lshlrev_b32_e32 v25, 2, v25
	v_lshlrev_b32_e32 v26, 2, v26
	v_lshlrev_b32_e32 v27, 2, v27
	v_lshlrev_b32_e32 v28, 2, v28
	v_lshlrev_b32_e32 v29, 2, v29
	v_lshlrev_b32_e32 v82, 2, v82
	v_lshlrev_b32_e32 v83, 2, v83
	global_load_dword v24, v24, s[4:5] nt
	s_nop 0
	global_load_dword v25, v25, s[4:5] nt
	s_nop 0
	global_load_dword v26, v26, s[4:5] nt
	s_nop 0
	global_load_dword v27, v27, s[4:5] nt
	s_nop 0
	global_load_dword v28, v28, s[4:5] nt
	s_nop 0
	global_load_dword v29, v29, s[4:5] nt
	s_nop 0
	global_load_dword v82, v82, s[4:5] nt
	s_nop 0
	global_load_dword v83, v83, s[4:5] nt
	v_or_b32_e32 v84, v6, v53
	v_or_b32_e32 v85, v6, v54
	v_or_b32_e32 v86, v6, v55
	v_or_b32_e32 v87, v6, v56
	v_or_b32_e32 v88, v6, v57
	v_or_b32_e32 v89, v6, v58
	v_or_b32_e32 v90, v6, v59
	v_or_b32_e32 v6, v6, v60
	v_lshlrev_b32_e32 v84, 2, v84
	v_lshlrev_b32_e32 v85, 2, v85
	v_lshlrev_b32_e32 v86, 2, v86
	v_lshlrev_b32_e32 v87, 2, v87
	v_lshlrev_b32_e32 v88, 2, v88
	v_lshlrev_b32_e32 v89, 2, v89
	v_lshlrev_b32_e32 v90, 2, v90
	v_lshlrev_b32_e32 v6, 2, v6
	global_load_dword v84, v84, s[4:5] nt
	s_nop 0
	global_load_dword v85, v85, s[4:5] nt
	s_nop 0
	global_load_dword v86, v86, s[4:5] nt
	s_nop 0
	global_load_dword v87, v87, s[4:5] nt
	s_nop 0
	global_load_dword v88, v88, s[4:5] nt
	s_nop 0
	global_load_dword v89, v89, s[4:5] nt
	s_nop 0
	global_load_dword v90, v90, s[4:5] nt
	s_nop 0
	global_load_dword v6, v6, s[4:5] nt
	s_lshl_b32 s4, s41, 1
	s_add_u32 s4, s38, s4
	s_addc_u32 s5, s39, 0
	s_waitcnt vmcnt(30)
	ds_write2_b32 v62, v8, v9 offset1:66
	s_waitcnt vmcnt(28)
	ds_write2_b32 v62, v10, v11 offset0:132 offset1:198
	s_waitcnt vmcnt(26)
	ds_write2_b32 v76, v12, v13 offset0:8 offset1:74
	s_waitcnt vmcnt(24)
	ds_write2_b32 v76, v14, v15 offset0:140 offset1:206
	s_waitcnt vmcnt(22)
	ds_write2_b32 v77, v16, v17 offset0:16 offset1:82
	s_waitcnt vmcnt(20)
	ds_write2_b32 v77, v18, v19 offset0:148 offset1:214
	s_waitcnt vmcnt(18)
	ds_write2_b32 v81, v20, v21 offset0:24 offset1:90
	s_waitcnt vmcnt(16)
	ds_write2_b32 v81, v22, v23 offset0:156 offset1:222
	v_add_u32_e32 v8, 0x1000, v62
	s_waitcnt vmcnt(14)
	ds_write2_b32 v8, v24, v25 offset0:32 offset1:98
	s_waitcnt vmcnt(12)
	ds_write2_b32 v8, v26, v27 offset0:164 offset1:230
	v_add_u32_e32 v8, 0x1400, v62
	s_waitcnt vmcnt(10)
	ds_write2_b32 v8, v28, v29 offset0:40 offset1:106
	s_waitcnt vmcnt(8)
	ds_write2_b32 v8, v82, v83 offset0:172 offset1:238
	v_add_u32_e32 v8, 0x1800, v62
	s_waitcnt vmcnt(6)
	ds_write2_b32 v8, v84, v85 offset0:48 offset1:114
	s_waitcnt vmcnt(4)
	ds_write2_b32 v8, v86, v87 offset0:180 offset1:246
	v_add_u32_e32 v8, 0x1c00, v62
	s_waitcnt vmcnt(2)
	ds_write2_b32 v8, v88, v89 offset0:56 offset1:122
	s_waitcnt vmcnt(0)
	ds_write2_b32 v8, v90, v6 offset0:188 offset1:254
	s_waitcnt lgkmcnt(0)
	ds_read2_b32 v[12:13], v64 offset0:33 offset1:41
	ds_read2_b32 v[14:15], v64 offset1:8
	ds_read2_b32 v[16:17], v64 offset0:66 offset1:74
	ds_read2_b32 v[18:19], v64 offset0:99 offset1:107
	ds_read2_b32 v[20:21], v64 offset0:132 offset1:140
	ds_read2_b32 v[22:23], v64 offset0:165 offset1:173
	ds_read2_b32 v[24:25], v64 offset0:198 offset1:206
	ds_read2_b32 v[26:27], v64 offset0:231 offset1:239
	v_lshlrev_b32_e32 v6, 1, v4
	v_lshl_add_u64 v[28:29], s[4:5], 0, v[6:7]
	v_or_b32_e32 v6, s30, v63
	v_lshlrev_b32_e32 v6, 11, v6
	s_waitcnt lgkmcnt(6)
	v_cvt_pk_bf16_f32 v8, v14, v12
	s_waitcnt lgkmcnt(4)
	v_cvt_pk_bf16_f32 v9, v16, v18
	s_waitcnt lgkmcnt(2)
	v_cvt_pk_bf16_f32 v10, v20, v22
	s_waitcnt lgkmcnt(0)
	v_cvt_pk_bf16_f32 v11, v24, v26
	v_lshl_add_u64 v[82:83], v[28:29], 0, v[6:7]
	global_store_dwordx4 v[82:83], v[8:11], off
	v_or_b32_e32 v6, s30, v65
	v_lshlrev_b32_e32 v6, 11, v6
	v_cvt_pk_bf16_f32 v8, v15, v13
	v_cvt_pk_bf16_f32 v9, v17, v19
	v_cvt_pk_bf16_f32 v10, v21, v23
	v_cvt_pk_bf16_f32 v11, v25, v27
	ds_read2_b32 v[14:15], v64 offset0:49 offset1:57
	ds_read2_b32 v[16:17], v64 offset0:16 offset1:24
	ds_read2_b32 v[18:19], v64 offset0:82 offset1:90
	ds_read2_b32 v[20:21], v64 offset0:115 offset1:123
	ds_read2_b32 v[22:23], v64 offset0:148 offset1:156
	ds_read2_b32 v[24:25], v64 offset0:181 offset1:189
	ds_read2_b32 v[26:27], v64 offset0:214 offset1:222
	ds_read2_b32 v[82:83], v64 offset0:247 offset1:255
	v_lshl_add_u64 v[12:13], v[28:29], 0, v[6:7]
	v_or_b32_e32 v6, s30, v66
	v_lshlrev_b32_e32 v6, 11, v6
	global_store_dwordx4 v[12:13], v[8:11], off
	v_lshl_add_u64 v[12:13], v[28:29], 0, v[6:7]
	v_or_b32_e32 v6, s30, v67
	s_waitcnt lgkmcnt(6)
	v_cvt_pk_bf16_f32 v8, v16, v14
	s_waitcnt lgkmcnt(4)
	v_cvt_pk_bf16_f32 v9, v18, v20
	s_waitcnt lgkmcnt(2)
	v_cvt_pk_bf16_f32 v10, v22, v24
	s_waitcnt lgkmcnt(0)
	v_cvt_pk_bf16_f32 v11, v26, v82
	v_lshlrev_b32_e32 v6, 11, v6
	global_store_dwordx4 v[12:13], v[8:11], off
	v_lshl_add_u64 v[12:13], v[28:29], 0, v[6:7]
	s_nop 0
	v_cvt_pk_bf16_f32 v8, v17, v15
	v_cvt_pk_bf16_f32 v9, v19, v21
	v_cvt_pk_bf16_f32 v10, v23, v25
	v_cvt_pk_bf16_f32 v11, v27, v83
	global_store_dwordx4 v[12:13], v[8:11], off
	s_waitcnt lgkmcnt(0)

.LBB0_70:
	s_cmpk_gt_u32 s38, 0x107f
	s_cselect_b64 s[4:5], -1, 0
	s_and_b64 s[38:39], s[4:5], exec
	s_cselect_b32 s38, 0x20c4000, 0
	s_add_u32 s38, s6, s38
	s_addc_u32 s39, s7, 0
	s_lshl_b32 s40, s40, 6
	s_and_b32 s42, s40, 0x3fc0
	v_cmp_lt_i32_e32 vcc, -1, v8
	v_or_b32_e32 v19, s42, v2
	v_mov_b32_e32 v9, 0
	v_mov_b32_e32 v10, 0
	s_and_saveexec_b64 s[40:41], vcc
	s_cbranch_execz .LBB0_72
	s_movk_i32 s43, 0x20c4
	v_mad_u32_u24 v6, v19, s43, v8
	v_lshl_add_u64 v[10:11], v[6:7], 2, s[38:39]
	global_load_dword v10, v[10:11], off nt
.LBB0_72:
	s_or_b64 exec, exec, s[40:41]
	v_mul_u32_u24_e32 v24, 0x20c4, v19
	s_and_saveexec_b64 s[40:41], vcc
	s_cbranch_execz .LBB0_74
	v_add3_u32 v6, v24, v8, s57
	v_lshl_add_u64 v[12:13], v[6:7], 2, s[38:39]
	global_load_dword v9, v[12:13], off nt
.LBB0_74:
	s_or_b64 exec, exec, s[40:41]
	v_mov_b32_e32 v11, 0
	v_mov_b32_e32 v12, 0
	s_and_saveexec_b64 s[40:41], vcc
	s_cbranch_execz .LBB0_76
	v_add3_u32 v6, v24, v8, s58
	v_lshl_add_u64 v[12:13], v[6:7], 2, s[38:39]
	global_load_dword v12, v[12:13], off nt
.LBB0_76:
	s_or_b64 exec, exec, s[40:41]
	s_and_saveexec_b64 s[40:41], vcc
	s_cbranch_execz .LBB0_78
	v_add3_u32 v6, v24, v8, s59
	v_lshl_add_u64 v[14:15], v[6:7], 2, s[38:39]
	global_load_dword v11, v[14:15], off nt
.LBB0_78:
	s_or_b64 exec, exec, s[40:41]
	v_mov_b32_e32 v13, 0
	v_mov_b32_e32 v14, 0
	s_and_saveexec_b64 s[40:41], vcc
	s_cbranch_execz .LBB0_80
	v_add3_u32 v6, v24, v8, s60
	v_lshl_add_u64 v[14:15], v[6:7], 2, s[38:39]
	global_load_dword v14, v[14:15], off nt
.LBB0_80:
	s_or_b64 exec, exec, s[40:41]
	s_and_saveexec_b64 s[40:41], vcc
	s_cbranch_execz .LBB0_82
	v_add3_u32 v6, v24, v8, s61
	v_lshl_add_u64 v[16:17], v[6:7], 2, s[38:39]
	global_load_dword v13, v[16:17], off nt
.LBB0_82:
	s_or_b64 exec, exec, s[40:41]
	v_mov_b32_e32 v15, 0
	v_mov_b32_e32 v16, 0
	s_and_saveexec_b64 s[40:41], vcc
	s_cbranch_execz .LBB0_84
	v_add3_u32 v6, v24, v8, s62
	v_lshl_add_u64 v[16:17], v[6:7], 2, s[38:39]
	global_load_dword v16, v[16:17], off nt
.LBB0_84:
	s_or_b64 exec, exec, s[40:41]
	s_and_saveexec_b64 s[40:41], vcc
	s_cbranch_execz .LBB0_86
	v_add3_u32 v6, v24, v8, s63
	v_lshl_add_u64 v[20:21], v[6:7], 2, s[38:39]
	global_load_dword v15, v[20:21], off nt
.LBB0_86:
	s_or_b64 exec, exec, s[40:41]
	v_mov_b32_e32 v17, 0
	v_mov_b32_e32 v18, 0
	s_and_saveexec_b64 s[40:41], vcc
	s_cbranch_execz .LBB0_88
	v_add3_u32 v6, v24, v8, s64
	v_lshl_add_u64 v[20:21], v[6:7], 2, s[38:39]
	global_load_dword v18, v[20:21], off nt
.LBB0_88:
	s_or_b64 exec, exec, s[40:41]
	s_and_saveexec_b64 s[40:41], vcc
	s_cbranch_execz .LBB0_90
	v_add3_u32 v6, v24, v8, s65
	v_lshl_add_u64 v[20:21], v[6:7], 2, s[38:39]
	global_load_dword v17, v[20:21], off nt
.LBB0_90:
	s_or_b64 exec, exec, s[40:41]
	v_mov_b32_e32 v20, 0
	v_mov_b32_e32 v21, 0
	s_and_saveexec_b64 s[40:41], vcc
	s_cbranch_execz .LBB0_92
	v_add3_u32 v6, v24, v8, s66
	v_lshl_add_u64 v[22:23], v[6:7], 2, s[38:39]
	global_load_dword v21, v[22:23], off nt
.LBB0_92:
	s_or_b64 exec, exec, s[40:41]
	s_and_saveexec_b64 s[40:41], vcc
	s_cbranch_execz .LBB0_94
	v_add3_u32 v6, v24, v8, s67
	v_lshl_add_u64 v[22:23], v[6:7], 2, s[38:39]
	global_load_dword v20, v[22:23], off nt
.LBB0_94:
	s_or_b64 exec, exec, s[40:41]
	v_mov_b32_e32 v22, 0
	v_mov_b32_e32 v23, 0
	s_and_saveexec_b64 s[40:41], vcc
	s_cbranch_execz .LBB0_96
	v_add3_u32 v6, v24, v8, s68
	v_lshl_add_u64 v[26:27], v[6:7], 2, s[38:39]
	global_load_dword v23, v[26:27], off nt
.LBB0_96:
	s_or_b64 exec, exec, s[40:41]
	s_and_saveexec_b64 s[40:41], vcc
	s_cbranch_execz .LBB0_98
	v_add3_u32 v6, v24, v8, s69
	v_lshl_add_u64 v[26:27], v[6:7], 2, s[38:39]
	global_load_dword v22, v[26:27], off nt
.LBB0_98:
	s_or_b64 exec, exec, s[40:41]
	v_mov_b32_e32 v25, 0
	v_mov_b32_e32 v26, 0
	s_and_saveexec_b64 s[40:41], vcc
	s_cbranch_execz .LBB0_100
	v_add3_u32 v6, v24, v8, s70
	v_lshl_add_u64 v[26:27], v[6:7], 2, s[38:39]
	global_load_dword v26, v[26:27], off nt
.LBB0_100:
	s_or_b64 exec, exec, s[40:41]
	s_and_saveexec_b64 s[40:41], vcc
	s_cbranch_execz .LBB0_102
	v_add3_u32 v6, v24, v8, s71
	v_lshl_add_u64 v[28:29], v[6:7], 2, s[38:39]
	global_load_dword v25, v[28:29], off nt
.LBB0_102:
	s_or_b64 exec, exec, s[40:41]
	v_mov_b32_e32 v27, 0
	v_mov_b32_e32 v28, 0
	s_and_saveexec_b64 s[40:41], vcc
	s_cbranch_execz .LBB0_104
	v_add3_u32 v6, v24, v8, s72
	v_lshl_add_u64 v[28:29], v[6:7], 2, s[38:39]
	global_load_dword v28, v[28:29], off nt
.LBB0_104:
	s_or_b64 exec, exec, s[40:41]
	s_and_saveexec_b64 s[40:41], vcc
	s_cbranch_execz .LBB0_106
	v_add3_u32 v6, v24, v8, s73
	v_lshl_add_u64 v[82:83], v[6:7], 2, s[38:39]
	global_load_dword v27, v[82:83], off nt
.LBB0_106:
	s_or_b64 exec, exec, s[40:41]
	v_mov_b32_e32 v29, 0
	v_mov_b32_e32 v82, 0
	s_and_saveexec_b64 s[40:41], vcc
	s_cbranch_execz .LBB0_108
	v_add3_u32 v6, v24, v8, s74
	v_lshl_add_u64 v[82:83], v[6:7], 2, s[38:39]
	global_load_dword v82, v[82:83], off nt
.LBB0_108:
	s_or_b64 exec, exec, s[40:41]
	s_and_saveexec_b64 s[40:41], vcc
	s_cbranch_execz .LBB0_110
	v_add3_u32 v6, v24, v8, s75
	v_lshl_add_u64 v[84:85], v[6:7], 2, s[38:39]
	global_load_dword v29, v[84:85], off nt
.LBB0_110:
	s_or_b64 exec, exec, s[40:41]
	v_mov_b32_e32 v83, 0
	v_mov_b32_e32 v84, 0
	s_and_saveexec_b64 s[40:41], vcc
	s_cbranch_execz .LBB0_112
	v_add3_u32 v6, v24, v8, s76
	v_lshl_add_u64 v[84:85], v[6:7], 2, s[38:39]
	global_load_dword v84, v[84:85], off nt
.LBB0_112:
	s_or_b64 exec, exec, s[40:41]
	s_and_saveexec_b64 s[40:41], vcc
	s_cbranch_execz .LBB0_114
	v_add3_u32 v6, v24, v8, s77
	v_lshl_add_u64 v[86:87], v[6:7], 2, s[38:39]
	global_load_dword v83, v[86:87], off nt
.LBB0_114:
	s_or_b64 exec, exec, s[40:41]
	v_mov_b32_e32 v85, 0
	v_mov_b32_e32 v86, 0
	s_and_saveexec_b64 s[40:41], vcc
	s_cbranch_execz .LBB0_116
	v_add3_u32 v6, v24, v8, s78
	v_lshl_add_u64 v[86:87], v[6:7], 2, s[38:39]
	global_load_dword v86, v[86:87], off nt
.LBB0_116:
	s_or_b64 exec, exec, s[40:41]
	s_and_saveexec_b64 s[40:41], vcc
	s_cbranch_execz .LBB0_118
	v_add3_u32 v6, v24, v8, s79
	v_lshl_add_u64 v[88:89], v[6:7], 2, s[38:39]
	global_load_dword v85, v[88:89], off nt
.LBB0_118:
	s_or_b64 exec, exec, s[40:41]
	v_mov_b32_e32 v87, 0
	v_mov_b32_e32 v88, 0
	s_and_saveexec_b64 s[40:41], vcc
	s_cbranch_execz .LBB0_120
	v_add3_u32 v6, v24, v8, s80
	v_lshl_add_u64 v[88:89], v[6:7], 2, s[38:39]
	global_load_dword v88, v[88:89], off nt
.LBB0_120:
	s_or_b64 exec, exec, s[40:41]
	s_and_saveexec_b64 s[40:41], vcc
	s_cbranch_execz .LBB0_122
	v_add3_u32 v6, v24, v8, s81
	v_lshl_add_u64 v[90:91], v[6:7], 2, s[38:39]
	global_load_dword v87, v[90:91], off nt
.LBB0_122:
	s_or_b64 exec, exec, s[40:41]
	v_mov_b32_e32 v89, 0
	v_mov_b32_e32 v91, 0
	s_and_saveexec_b64 s[40:41], vcc
	s_cbranch_execz .LBB0_124
	v_add3_u32 v6, v24, v8, s82
	v_lshl_add_u64 v[90:91], v[6:7], 2, s[38:39]
	global_load_dword v91, v[90:91], off nt
.LBB0_124:
	s_or_b64 exec, exec, s[40:41]
	s_and_saveexec_b64 s[40:41], vcc
	s_cbranch_execz .LBB0_126
	v_add3_u32 v6, v24, v8, s83
	v_lshl_add_u64 v[92:93], v[6:7], 2, s[38:39]
	global_load_dword v89, v[92:93], off nt
.LBB0_126:
	s_or_b64 exec, exec, s[40:41]
	v_mov_b32_e32 v92, 0
	v_mov_b32_e32 v93, 0
	s_and_saveexec_b64 s[40:41], vcc
	s_cbranch_execz .LBB0_128
	v_add3_u32 v6, v24, v8, s84
	v_lshl_add_u64 v[94:95], v[6:7], 2, s[38:39]
	global_load_dword v93, v[94:95], off nt
.LBB0_128:
	s_or_b64 exec, exec, s[40:41]
	s_and_saveexec_b64 s[40:41], vcc
	s_cbranch_execz .LBB0_130
	v_add3_u32 v6, v24, v8, s85
	v_lshl_add_u64 v[94:95], v[6:7], 2, s[38:39]
	global_load_dword v92, v[94:95], off nt
.LBB0_130:
	s_or_b64 exec, exec, s[40:41]
	v_mov_b32_e32 v90, 0
	v_mov_b32_e32 v94, 0
	s_and_saveexec_b64 s[40:41], vcc
	s_cbranch_execz .LBB0_132
	v_add3_u32 v6, v24, v8, s86
	v_lshl_add_u64 v[94:95], v[6:7], 2, s[38:39]
	global_load_dword v94, v[94:95], off nt
.LBB0_132:
	s_or_b64 exec, exec, s[40:41]
	s_and_saveexec_b64 s[40:41], vcc
	s_cbranch_execz .LBB0_134
	v_add3_u32 v6, v24, v8, s87
	v_lshl_add_u64 v[96:97], v[6:7], 2, s[38:39]
	global_load_dword v90, v[96:97], off nt
.LBB0_134:
	s_or_b64 exec, exec, s[40:41]
	s_and_b64 s[38:39], s[4:5], exec
	s_movk_i32 s38, 0x4000
	s_cselect_b32 s38, s38, 0x1000
	s_add_u32 s38, s26, s38
	s_addc_u32 s39, s27, 0
	v_lshlrev_b32_e32 v6, 2, v19
	v_add_lshl_u32 v8, v2, s42, 2
	global_load_dword v6, v6, s[38:39] nt
	s_nop 0
	global_load_dword v19, v8, s[38:39] offset:8 nt
	global_load_dword v24, v8, s[38:39] offset:16 nt
	global_load_dword v95, v8, s[38:39] offset:24 nt
	global_load_dword v96, v8, s[38:39] offset:32 nt
	global_load_dword v97, v8, s[38:39] offset:40 nt
	global_load_dword v98, v8, s[38:39] offset:48 nt
	global_load_dword v99, v8, s[38:39] offset:56 nt
	global_load_dword v100, v8, s[38:39] offset:64 nt
	global_load_dword v101, v8, s[38:39] offset:72 nt
	global_load_dword v102, v8, s[38:39] offset:80 nt
	global_load_dword v103, v8, s[38:39] offset:88 nt
	global_load_dword v104, v8, s[38:39] offset:96 nt
	global_load_dword v105, v8, s[38:39] offset:104 nt
	global_load_dword v106, v8, s[38:39] offset:112 nt
	global_load_dword v107, v8, s[38:39] offset:120 nt
	global_load_dword v108, v8, s[38:39] offset:128 nt
	global_load_dword v109, v8, s[38:39] offset:136 nt
	global_load_dword v110, v8, s[38:39] offset:144 nt
	global_load_dword v111, v8, s[38:39] offset:152 nt
	global_load_dword v112, v8, s[38:39] offset:160 nt
	global_load_dword v113, v8, s[38:39] offset:168 nt
	global_load_dword v114, v8, s[38:39] offset:176 nt
	global_load_dword v115, v8, s[38:39] offset:184 nt
	global_load_dword v116, v8, s[38:39] offset:192 nt
	global_load_dword v117, v8, s[38:39] offset:200 nt
	global_load_dword v118, v8, s[38:39] offset:208 nt
	global_load_dword v119, v8, s[38:39] offset:216 nt
	global_load_dword v120, v8, s[38:39] offset:224 nt
	global_load_dword v121, v8, s[38:39] offset:232 nt
	global_load_dword v122, v8, s[38:39] offset:240 nt
	s_nop 0
	global_load_dword v8, v8, s[38:39] offset:248 nt
	v_add_u32_e32 v123, v61, v70
	v_add_u32_e32 v125, v61, v71
	v_add_u32_e32 v124, 0x400, v72
	v_add_u32_e32 v126, 0x400, v123
	v_add_u32_e32 v127, 0x400, v125
	v_add_u32_e32 v128, 0x800, v125
	s_and_b64 s[4:5], s[4:5], exec
	s_cselect_b32 s4, 0x1080000, 0
	s_add_u32 s4, s51, s4
	s_addc_u32 s5, s52, 0
	s_lshl_b32 s38, s42, 1
	s_add_u32 s4, s4, s38
	s_addc_u32 s5, s5, 0
	s_waitcnt vmcnt(31)
	v_mul_f32_e32 v6, v10, v6
	s_waitcnt vmcnt(30)
	v_mul_f32_e32 v9, v9, v19
	s_waitcnt vmcnt(29)
	v_mul_f32_e32 v10, v12, v24
	s_waitcnt vmcnt(28)
	v_mul_f32_e32 v11, v11, v95
	s_waitcnt vmcnt(27)
	v_mul_f32_e32 v12, v14, v96
	s_waitcnt vmcnt(26)
	v_mul_f32_e32 v13, v13, v97
	s_waitcnt vmcnt(25)
	v_mul_f32_e32 v14, v16, v98
	s_waitcnt vmcnt(24)
	v_mul_f32_e32 v15, v15, v99
	s_waitcnt vmcnt(23)
	v_mul_f32_e32 v16, v18, v100
	s_waitcnt vmcnt(22)
	v_mul_f32_e32 v17, v17, v101
	s_waitcnt vmcnt(21)
	v_mul_f32_e32 v18, v21, v102
	s_waitcnt vmcnt(20)
	v_mul_f32_e32 v19, v20, v103
	s_waitcnt vmcnt(19)
	v_mul_f32_e32 v20, v23, v104
	s_waitcnt vmcnt(18)
	v_mul_f32_e32 v21, v22, v105
	s_waitcnt vmcnt(17)
	v_mul_f32_e32 v22, v26, v106
	s_waitcnt vmcnt(16)
	v_mul_f32_e32 v23, v25, v107
	s_waitcnt vmcnt(15)
	v_mul_f32_e32 v24, v28, v108
	s_waitcnt vmcnt(14)
	v_mul_f32_e32 v25, v27, v109
	s_waitcnt vmcnt(13)
	v_mul_f32_e32 v26, v82, v110
	s_waitcnt vmcnt(12)
	v_mul_f32_e32 v27, v29, v111
	s_waitcnt vmcnt(11)
	v_mul_f32_e32 v28, v84, v112
	s_waitcnt vmcnt(10)
	v_mul_f32_e32 v29, v83, v113
	s_waitcnt vmcnt(9)
	v_mul_f32_e32 v82, v86, v114
	s_waitcnt vmcnt(8)
	v_mul_f32_e32 v83, v85, v115
	s_waitcnt vmcnt(7)
	v_mul_f32_e32 v84, v88, v116
	ds_write_b32 v62, v6
	ds_write2_b32 v123, v9, v10 offset1:66
	ds_write2_b32 v123, v11, v12 offset0:132 offset1:198
	ds_write2_b32 v126, v13, v14 offset0:8 offset1:74
	ds_write2_b32 v72, v15, v16 offset1:66
	ds_write2_b32 v72, v17, v18 offset0:132 offset1:198
	ds_write2_b32 v124, v19, v20 offset0:8 offset1:74
	ds_write2_b32 v125, v21, v22 offset1:66
	ds_write2_b32 v125, v23, v24 offset0:132 offset1:198
	ds_write2_b32 v127, v25, v26 offset0:8 offset1:74
	ds_write2_b32 v127, v27, v28 offset0:140 offset1:206
	ds_write2_b32 v128, v29, v82 offset0:16 offset1:82
	ds_write2_b32 v128, v83, v84 offset0:148 offset1:214
	s_waitcnt vmcnt(6)
	v_mul_f32_e32 v6, v87, v117
	s_waitcnt vmcnt(5)
	v_mul_f32_e32 v9, v91, v118
	v_add_u32_e32 v10, 0xc00, v125
	ds_write2_b32 v10, v6, v9 offset0:24 offset1:90
	s_waitcnt vmcnt(4)
	v_mul_f32_e32 v6, v89, v119
	s_waitcnt vmcnt(3)
	v_mul_f32_e32 v9, v93, v120
	ds_write2_b32 v10, v6, v9 offset0:156 offset1:222
	s_waitcnt vmcnt(2)
	v_mul_f32_e32 v6, v92, v121
	s_waitcnt vmcnt(1)
	v_mul_f32_e32 v9, v94, v122
	v_add_u32_e32 v10, 0x1000, v125
	ds_write2_b32 v10, v6, v9 offset0:32 offset1:98
	s_waitcnt vmcnt(0)
	v_mul_f32_e32 v6, v90, v8
	ds_write_b32 v125, v6 offset:4752
	s_waitcnt lgkmcnt(0)
	ds_read2_b32 v[12:13], v64 offset0:33 offset1:41
	ds_read2_b32 v[14:15], v64 offset1:8
	ds_read2_b32 v[16:17], v64 offset0:66 offset1:74
	ds_read2_b32 v[18:19], v64 offset0:99 offset1:107
	ds_read2_b32 v[20:21], v64 offset0:132 offset1:140
	ds_read2_b32 v[22:23], v64 offset0:165 offset1:173
	ds_read2_b32 v[24:25], v64 offset0:198 offset1:206
	ds_read2_b32 v[26:27], v64 offset0:231 offset1:239
	v_lshlrev_b32_e32 v6, 1, v4
	v_lshl_add_u64 v[28:29], s[4:5], 0, v[6:7]
	v_or_b32_e32 v6, s30, v63
	v_lshlrev_b32_e32 v6, 11, v6
	s_waitcnt lgkmcnt(6)
	v_cvt_pk_bf16_f32 v8, v14, v12
	s_waitcnt lgkmcnt(4)
	v_cvt_pk_bf16_f32 v9, v16, v18
	s_waitcnt lgkmcnt(2)
	v_cvt_pk_bf16_f32 v10, v20, v22
	s_waitcnt lgkmcnt(0)
	v_cvt_pk_bf16_f32 v11, v24, v26
	v_lshl_add_u64 v[82:83], v[28:29], 0, v[6:7]
	global_store_dwordx4 v[82:83], v[8:11], off
	v_or_b32_e32 v6, s30, v65
	v_lshlrev_b32_e32 v6, 11, v6
	v_cvt_pk_bf16_f32 v8, v15, v13
	v_cvt_pk_bf16_f32 v9, v17, v19
	v_cvt_pk_bf16_f32 v10, v21, v23
	v_cvt_pk_bf16_f32 v11, v25, v27
	ds_read2_b32 v[14:15], v64 offset0:49 offset1:57
	ds_read2_b32 v[16:17], v64 offset0:16 offset1:24
	ds_read2_b32 v[18:19], v64 offset0:82 offset1:90
	ds_read2_b32 v[20:21], v64 offset0:115 offset1:123
	ds_read2_b32 v[22:23], v64 offset0:148 offset1:156
	ds_read2_b32 v[24:25], v64 offset0:181 offset1:189
	ds_read2_b32 v[26:27], v64 offset0:214 offset1:222
	ds_read2_b32 v[82:83], v64 offset0:247 offset1:255
	v_lshl_add_u64 v[12:13], v[28:29], 0, v[6:7]
	v_or_b32_e32 v6, s30, v66
	v_lshlrev_b32_e32 v6, 11, v6
	global_store_dwordx4 v[12:13], v[8:11], off
	v_lshl_add_u64 v[12:13], v[28:29], 0, v[6:7]
	v_or_b32_e32 v6, s30, v67
	s_waitcnt lgkmcnt(6)
	v_cvt_pk_bf16_f32 v8, v16, v14
	s_waitcnt lgkmcnt(4)
	v_cvt_pk_bf16_f32 v9, v18, v20
	s_waitcnt lgkmcnt(2)
	v_cvt_pk_bf16_f32 v10, v22, v24
	s_waitcnt lgkmcnt(0)
	v_cvt_pk_bf16_f32 v11, v26, v82
	v_lshlrev_b32_e32 v6, 11, v6
	global_store_dwordx4 v[12:13], v[8:11], off
	v_lshl_add_u64 v[12:13], v[28:29], 0, v[6:7]
	s_nop 0
	v_cvt_pk_bf16_f32 v8, v17, v15
	v_cvt_pk_bf16_f32 v9, v19, v21
	v_cvt_pk_bf16_f32 v10, v23, v25
	v_cvt_pk_bf16_f32 v11, v27, v83
	global_store_dwordx4 v[12:13], v[8:11], off
	s_waitcnt lgkmcnt(0)

.LBB0_136:
	s_andn2_b64 vcc, exec, s[4:5]
	s_cbranch_vccnz .LBB0_138
	s_add_i32 s30, s88, 0xd400
	s_and_b32 s4, s30, 0xffff
	s_mul_i32 s4, s4, 0xba2f
	s_lshr_b32 s38, s4, 26
	s_mul_i32 s4, s38, 0xb00000
	s_add_u32 s4, s34, s4
	s_addc_u32 s5, s35, 0
	s_mul_i32 s39, s38, 0x580000
	s_add_u32 s39, s53, s39
	s_mulk_i32 s38, 0x580
	s_addc_u32 s40, s54, 0
	s_sub_i32 s30, s30, s38
	s_and_b32 s30, s30, 0xffff
	s_lshl_b32 s38, s30, 1
	s_and_b32 s38, s38, 0xfc0
	s_lshl_b32 s30, s30, 5
	s_and_b32 s30, s30, 0x3e0
	v_or_b32_e32 v6, s38, v2
	v_lshl_or_b32 v6, v6, 10, s30
	v_or_b32_e32 v8, v6, v40
	v_or_b32_e32 v9, v6, v5
	v_or_b32_e32 v10, v6, v30
	v_or_b32_e32 v11, v6, v31
	v_or_b32_e32 v12, v6, v32
	v_or_b32_e32 v13, v6, v33
	v_or_b32_e32 v14, v6, v34
	v_or_b32_e32 v15, v6, v35
	v_or_b32_e32 v16, v6, v36
	v_or_b32_e32 v17, v6, v37
	v_or_b32_e32 v18, v6, v38
	v_or_b32_e32 v19, v6, v39
	v_or_b32_e32 v20, v6, v41
	v_or_b32_e32 v21, v6, v42
	v_or_b32_e32 v22, v6, v43
	v_or_b32_e32 v23, v6, v44
	v_lshlrev_b32_e32 v8, 2, v8
	v_lshlrev_b32_e32 v9, 2, v9
	v_lshlrev_b32_e32 v10, 2, v10
	v_lshlrev_b32_e32 v11, 2, v11
	v_lshlrev_b32_e32 v12, 2, v12
	v_lshlrev_b32_e32 v13, 2, v13
	v_lshlrev_b32_e32 v14, 2, v14
	v_lshlrev_b32_e32 v15, 2, v15
	v_lshlrev_b32_e32 v16, 2, v16
	v_lshlrev_b32_e32 v17, 2, v17
	v_lshlrev_b32_e32 v18, 2, v18
	v_lshlrev_b32_e32 v19, 2, v19
	v_lshlrev_b32_e32 v20, 2, v20
	v_lshlrev_b32_e32 v21, 2, v21
	v_lshlrev_b32_e32 v22, 2, v22
	v_lshlrev_b32_e32 v23, 2, v23
	global_load_dword v8, v8, s[4:5] nt
	s_nop 0
	global_load_dword v9, v9, s[4:5] nt
	s_nop 0
	global_load_dword v10, v10, s[4:5] nt
	s_nop 0
	global_load_dword v11, v11, s[4:5] nt
	s_nop 0
	global_load_dword v12, v12, s[4:5] nt
	s_nop 0
	global_load_dword v13, v13, s[4:5] nt
	s_nop 0
	global_load_dword v14, v14, s[4:5] nt
	s_nop 0
	global_load_dword v15, v15, s[4:5] nt
	s_nop 0
	global_load_dword v16, v16, s[4:5] nt
	s_nop 0
	global_load_dword v17, v17, s[4:5] nt
	s_nop 0
	global_load_dword v18, v18, s[4:5] nt
	s_nop 0
	global_load_dword v19, v19, s[4:5] nt
	s_nop 0
	global_load_dword v20, v20, s[4:5] nt
	s_nop 0
	global_load_dword v21, v21, s[4:5] nt
	s_nop 0
	global_load_dword v22, v22, s[4:5] nt
	s_nop 0
	global_load_dword v23, v23, s[4:5] nt
	v_or_b32_e32 v24, v6, v45
	v_or_b32_e32 v25, v6, v46
	v_or_b32_e32 v26, v6, v47
	v_or_b32_e32 v27, v6, v48
	v_or_b32_e32 v28, v6, v49
	v_or_b32_e32 v29, v6, v50
	v_or_b32_e32 v82, v6, v51
	v_or_b32_e32 v83, v6, v52
	v_lshlrev_b32_e32 v24, 2, v24
	v_lshlrev_b32_e32 v25, 2, v25
	v_lshlrev_b32_e32 v26, 2, v26
	v_lshlrev_b32_e32 v27, 2, v27
	v_lshlrev_b32_e32 v28, 2, v28
	v_lshlrev_b32_e32 v29, 2, v29
	v_lshlrev_b32_e32 v82, 2, v82
	v_lshlrev_b32_e32 v83, 2, v83
	global_load_dword v24, v24, s[4:5] nt
	s_nop 0
	global_load_dword v25, v25, s[4:5] nt
	s_nop 0
	global_load_dword v26, v26, s[4:5] nt
	s_nop 0
	global_load_dword v27, v27, s[4:5] nt
	s_nop 0
	global_load_dword v28, v28, s[4:5] nt
	s_nop 0
	global_load_dword v29, v29, s[4:5] nt
	s_nop 0
	global_load_dword v82, v82, s[4:5] nt
	s_nop 0
	global_load_dword v83, v83, s[4:5] nt
	v_or_b32_e32 v84, v6, v53
	v_or_b32_e32 v85, v6, v54
	v_or_b32_e32 v86, v6, v55
	v_or_b32_e32 v87, v6, v56
	v_or_b32_e32 v88, v6, v57
	v_or_b32_e32 v89, v6, v58
	v_or_b32_e32 v90, v6, v59
	v_or_b32_e32 v6, v6, v60
	v_lshlrev_b32_e32 v84, 2, v84
	v_lshlrev_b32_e32 v85, 2, v85
	v_lshlrev_b32_e32 v86, 2, v86
	v_lshlrev_b32_e32 v87, 2, v87
	v_lshlrev_b32_e32 v88, 2, v88
	v_lshlrev_b32_e32 v89, 2, v89
	v_lshlrev_b32_e32 v90, 2, v90
	v_lshlrev_b32_e32 v6, 2, v6
	global_load_dword v84, v84, s[4:5] nt
	s_nop 0
	global_load_dword v85, v85, s[4:5] nt
	s_nop 0
	global_load_dword v86, v86, s[4:5] nt
	s_nop 0
	global_load_dword v87, v87, s[4:5] nt
	s_nop 0
	global_load_dword v88, v88, s[4:5] nt
	s_nop 0
	global_load_dword v89, v89, s[4:5] nt
	s_nop 0
	global_load_dword v90, v90, s[4:5] nt
	s_nop 0
	global_load_dword v6, v6, s[4:5] nt
	s_lshl_b32 s4, s38, 1
	s_add_u32 s4, s39, s4
	s_addc_u32 s5, s40, 0
	s_waitcnt vmcnt(30)
	ds_write2_b32 v62, v8, v9 offset1:66
	s_waitcnt vmcnt(28)
	ds_write2_b32 v62, v10, v11 offset0:132 offset1:198
	s_waitcnt vmcnt(26)
	ds_write2_b32 v76, v12, v13 offset0:8 offset1:74
	s_waitcnt vmcnt(24)
	ds_write2_b32 v76, v14, v15 offset0:140 offset1:206
	s_waitcnt vmcnt(22)
	ds_write2_b32 v77, v16, v17 offset0:16 offset1:82
	s_waitcnt vmcnt(20)
	ds_write2_b32 v77, v18, v19 offset0:148 offset1:214
	s_waitcnt vmcnt(18)
	ds_write2_b32 v81, v20, v21 offset0:24 offset1:90
	s_waitcnt vmcnt(16)
	ds_write2_b32 v81, v22, v23 offset0:156 offset1:222
	v_add_u32_e32 v8, 0x1000, v62
	s_waitcnt vmcnt(14)
	ds_write2_b32 v8, v24, v25 offset0:32 offset1:98
	s_waitcnt vmcnt(12)
	ds_write2_b32 v8, v26, v27 offset0:164 offset1:230
	v_add_u32_e32 v8, 0x1400, v62
	s_waitcnt vmcnt(10)
	ds_write2_b32 v8, v28, v29 offset0:40 offset1:106
	s_waitcnt vmcnt(8)
	ds_write2_b32 v8, v82, v83 offset0:172 offset1:238
	v_add_u32_e32 v8, 0x1800, v62
	s_waitcnt vmcnt(6)
	ds_write2_b32 v8, v84, v85 offset0:48 offset1:114
	s_waitcnt vmcnt(4)
	ds_write2_b32 v8, v86, v87 offset0:180 offset1:246
	v_add_u32_e32 v8, 0x1c00, v62
	s_waitcnt vmcnt(2)
	ds_write2_b32 v8, v88, v89 offset0:56 offset1:122
	s_waitcnt vmcnt(0)
	ds_write2_b32 v8, v90, v6 offset0:188 offset1:254
	s_waitcnt lgkmcnt(0)
	v_lshlrev_b32_e32 v6, 1, v4
	ds_read2_b32 v[12:13], v64 offset0:33 offset1:41
	ds_read2_b32 v[14:15], v64 offset1:8
	ds_read2_b32 v[16:17], v64 offset0:66 offset1:74
	ds_read2_b32 v[18:19], v64 offset0:99 offset1:107
	ds_read2_b32 v[20:21], v64 offset0:132 offset1:140
	ds_read2_b32 v[22:23], v64 offset0:165 offset1:173
	ds_read2_b32 v[24:25], v64 offset0:198 offset1:206
	ds_read2_b32 v[26:27], v64 offset0:231 offset1:239
	v_lshl_add_u64 v[28:29], s[4:5], 0, v[6:7]
	v_or_b32_e32 v6, s30, v63
	v_mul_u32_u24_e32 v6, 0xb00, v6
	v_lshlrev_b32_e32 v6, 1, v6
	v_lshl_add_u64 v[82:83], v[28:29], 0, v[6:7]
	v_or_b32_e32 v6, s30, v65
	s_waitcnt lgkmcnt(6)
	v_cvt_pk_bf16_f32 v8, v14, v12
	s_waitcnt lgkmcnt(4)
	v_cvt_pk_bf16_f32 v9, v16, v18
	s_waitcnt lgkmcnt(2)
	v_cvt_pk_bf16_f32 v10, v20, v22
	s_waitcnt lgkmcnt(0)
	v_cvt_pk_bf16_f32 v11, v24, v26
	v_mul_u32_u24_e32 v6, 0xb00, v6
	global_store_dwordx4 v[82:83], v[8:11], off
	v_lshlrev_b32_e32 v6, 1, v6
	s_nop 0
	v_cvt_pk_bf16_f32 v8, v15, v13
	v_cvt_pk_bf16_f32 v9, v17, v19
	v_cvt_pk_bf16_f32 v10, v21, v23
	v_cvt_pk_bf16_f32 v11, v25, v27
	v_lshl_add_u64 v[12:13], v[28:29], 0, v[6:7]
	ds_read2_b32 v[14:15], v64 offset0:16 offset1:24
	ds_read2_b32 v[16:17], v64 offset0:49 offset1:57
	ds_read2_b32 v[18:19], v64 offset0:82 offset1:90
	ds_read2_b32 v[20:21], v64 offset0:115 offset1:123
	ds_read2_b32 v[22:23], v64 offset0:148 offset1:156
	ds_read2_b32 v[24:25], v64 offset0:181 offset1:189
	ds_read2_b32 v[26:27], v64 offset0:214 offset1:222
	ds_read2_b32 v[82:83], v64 offset0:247 offset1:255
	v_or_b32_e32 v6, s30, v66
	v_mul_u32_u24_e32 v6, 0xb00, v6
	v_lshlrev_b32_e32 v6, 1, v6
	global_store_dwordx4 v[12:13], v[8:11], off
	v_lshl_add_u64 v[12:13], v[28:29], 0, v[6:7]
	v_or_b32_e32 v6, s30, v67
	v_mul_u32_u24_e32 v6, 0xb00, v6
	s_waitcnt lgkmcnt(6)
	v_cvt_pk_bf16_f32 v8, v14, v16
	s_waitcnt lgkmcnt(4)
	v_cvt_pk_bf16_f32 v9, v18, v20
	s_waitcnt lgkmcnt(2)
	v_cvt_pk_bf16_f32 v10, v22, v24
	s_waitcnt lgkmcnt(0)
	v_cvt_pk_bf16_f32 v11, v26, v82
	v_lshlrev_b32_e32 v6, 1, v6
	global_store_dwordx4 v[12:13], v[8:11], off
	v_lshl_add_u64 v[12:13], v[28:29], 0, v[6:7]
	s_nop 0
	v_cvt_pk_bf16_f32 v8, v15, v17
	v_cvt_pk_bf16_f32 v9, v19, v21
	v_cvt_pk_bf16_f32 v10, v23, v25
	v_cvt_pk_bf16_f32 v11, v27, v83
	global_store_dwordx4 v[12:13], v[8:11], off
	s_waitcnt lgkmcnt(0)

.LBB0_140:
	s_mul_hi_i32 s4, s88, 0x2e8ba2e9
	s_lshr_b32 s5, s4, 31
	s_ashr_i32 s89, s4, 9
	s_add_i32 s89, s89, s5
	s_mul_i32 s5, s89, 0x1600000
	s_mul_hi_i32 s4, s89, 0x1600000
	s_add_u32 s40, s22, s5
	s_addc_u32 s41, s23, s4
	s_mul_i32 s4, s89, 0xfffff500
	s_add_i32 s4, s88, s4
	s_mul_i32 s5, s4, 0xba3
	s_lshr_b32 s30, s5, 31
	s_ashr_i32 s5, s5, 19
	s_add_i32 s5, s5, s30
	s_mul_i32 s30, s5, 0xb0
	s_sub_i32 s4, s4, s30
	s_sext_i32_i16 s4, s4
	s_lshl_b32 s30, s4, 5
	s_lshl_b32 s38, s5, 6
	s_and_b32 s5, s30, 0xe0
	s_cmpk_lt_u32 s5, 0x80
	s_cselect_b64 vcc, -1, 0
	s_lshl_b32 s4, s4, 4
	v_or_b32_e32 v6, s5, v40
	s_and_b32 s4, s4, 0xffffff80
	v_or_b32_e32 v8, s4, v6
	s_addk_i32 s4, 0xa80
	v_add_u32_e32 v6, s4, v6
	v_or_b32_e32 v10, s38, v2
	v_cndmask_b32_e32 v6, v6, v8, vcc
	v_mul_i32_i24_e32 v16, 0x5800, v10
	v_cmp_lt_i32_e64 s[4:5], -1, v6
	v_lshl_add_u64 v[14:15], v[6:7], 2, s[40:41]
	v_mov_b32_e32 v82, 0
	v_ashrrev_i32_e32 v17, 31, v16
	v_mov_b32_e32 v6, 0
	s_and_saveexec_b64 s[40:41], s[4:5]
	s_cbranch_execz .LBB0_142
	v_lshl_add_u64 v[8:9], v[14:15], 0, v[16:17]
	global_load_dword v6, v[8:9], off nt
.LBB0_142:
	s_or_b64 exec, exec, s[40:41]
	s_and_saveexec_b64 s[40:41], s[4:5]
	s_cbranch_execz .LBB0_144
	v_lshl_add_u64 v[8:9], v[14:15], 0, v[16:17]
	v_add_co_u32_e32 v8, vcc, 0xb000, v8
	s_nop 1
	v_addc_co_u32_e32 v9, vcc, 0, v9, vcc
	global_load_dword v82, v[8:9], off nt
.LBB0_144:
	s_or_b64 exec, exec, s[40:41]
	v_mov_b32_e32 v9, 0
	v_mov_b32_e32 v8, 0
	s_and_saveexec_b64 s[40:41], s[4:5]
	s_cbranch_execz .LBB0_146
	v_lshl_add_u64 v[12:13], v[14:15], 0, v[16:17]
	v_add_co_u32_e32 v12, vcc, 0x16000, v12
	s_nop 1
	v_addc_co_u32_e32 v13, vcc, 0, v13, vcc
	global_load_dword v8, v[12:13], off nt
.LBB0_146:
	s_or_b64 exec, exec, s[40:41]
	s_and_saveexec_b64 s[40:41], s[4:5]
	s_cbranch_execz .LBB0_148
	v_lshl_add_u64 v[12:13], v[14:15], 0, v[16:17]
	v_add_co_u32_e32 v12, vcc, 0x21000, v12
	s_nop 1
	v_addc_co_u32_e32 v13, vcc, 0, v13, vcc
	global_load_dword v9, v[12:13], off nt
.LBB0_148:
	s_or_b64 exec, exec, s[40:41]
	v_mov_b32_e32 v83, 0
	v_mov_b32_e32 v84, 0
	s_and_saveexec_b64 s[40:41], s[4:5]
	s_cbranch_execz .LBB0_150
	v_lshl_add_u64 v[12:13], v[14:15], 0, v[16:17]
	v_add_co_u32_e32 v12, vcc, 0x2c000, v12
	s_nop 1
	v_addc_co_u32_e32 v13, vcc, 0, v13, vcc
	global_load_dword v84, v[12:13], off nt
.LBB0_150:
	s_or_b64 exec, exec, s[40:41]
	s_and_saveexec_b64 s[40:41], s[4:5]
	s_cbranch_execz .LBB0_152
	v_lshl_add_u64 v[12:13], v[14:15], 0, v[16:17]
	v_add_co_u32_e32 v12, vcc, 0x37000, v12
	s_nop 1
	v_addc_co_u32_e32 v13, vcc, 0, v13, vcc
	global_load_dword v83, v[12:13], off nt
.LBB0_152:
	s_or_b64 exec, exec, s[40:41]
	v_mov_b32_e32 v13, 0
	v_mov_b32_e32 v12, 0
	s_and_saveexec_b64 s[40:41], s[4:5]
	s_cbranch_execz .LBB0_154
	v_lshl_add_u64 v[18:19], v[14:15], 0, v[16:17]
	v_add_co_u32_e32 v18, vcc, 0x42000, v18
	s_nop 1
	v_addc_co_u32_e32 v19, vcc, 0, v19, vcc
	global_load_dword v12, v[18:19], off nt
.LBB0_154:
	s_or_b64 exec, exec, s[40:41]
	s_and_saveexec_b64 s[40:41], s[4:5]
	s_cbranch_execz .LBB0_156
	v_lshl_add_u64 v[18:19], v[14:15], 0, v[16:17]
	v_add_co_u32_e32 v18, vcc, 0x4d000, v18
	s_nop 1
	v_addc_co_u32_e32 v19, vcc, 0, v19, vcc
	global_load_dword v13, v[18:19], off nt
.LBB0_156:
	s_or_b64 exec, exec, s[40:41]
	v_mov_b32_e32 v85, 0
	v_mov_b32_e32 v86, 0
	s_and_saveexec_b64 s[40:41], s[4:5]
	s_cbranch_execz .LBB0_158
	v_lshl_add_u64 v[18:19], v[14:15], 0, v[16:17]
	v_add_co_u32_e32 v18, vcc, 0x58000, v18
	s_nop 1
	v_addc_co_u32_e32 v19, vcc, 0, v19, vcc
	global_load_dword v86, v[18:19], off nt
.LBB0_158:
	s_or_b64 exec, exec, s[40:41]
	s_and_saveexec_b64 s[40:41], s[4:5]
	s_cbranch_execz .LBB0_160
	v_lshl_add_u64 v[18:19], v[14:15], 0, v[16:17]
	v_add_co_u32_e32 v18, vcc, 0x63000, v18
	s_nop 1
	v_addc_co_u32_e32 v19, vcc, 0, v19, vcc
	global_load_dword v85, v[18:19], off nt
.LBB0_160:
	s_or_b64 exec, exec, s[40:41]
	v_mov_b32_e32 v19, 0
	v_mov_b32_e32 v18, 0
	s_and_saveexec_b64 s[40:41], s[4:5]
	s_cbranch_execz .LBB0_162
	v_lshl_add_u64 v[20:21], v[14:15], 0, v[16:17]
	v_add_co_u32_e32 v20, vcc, 0x6e000, v20
	s_nop 1
	v_addc_co_u32_e32 v21, vcc, 0, v21, vcc
	global_load_dword v18, v[20:21], off nt
.LBB0_162:
	s_or_b64 exec, exec, s[40:41]
	s_and_saveexec_b64 s[40:41], s[4:5]
	s_cbranch_execz .LBB0_164
	v_lshl_add_u64 v[20:21], v[14:15], 0, v[16:17]
	v_add_co_u32_e32 v20, vcc, 0x79000, v20
	s_nop 1
	v_addc_co_u32_e32 v21, vcc, 0, v21, vcc
	global_load_dword v19, v[20:21], off nt
.LBB0_164:
	s_or_b64 exec, exec, s[40:41]
	v_mov_b32_e32 v87, 0
	v_mov_b32_e32 v88, 0
	s_and_saveexec_b64 s[40:41], s[4:5]
	s_cbranch_execz .LBB0_166
	v_lshl_add_u64 v[20:21], v[14:15], 0, v[16:17]
	v_add_co_u32_e32 v20, vcc, 0x84000, v20
	s_nop 1
	v_addc_co_u32_e32 v21, vcc, 0, v21, vcc
	global_load_dword v88, v[20:21], off nt
.LBB0_166:
	s_or_b64 exec, exec, s[40:41]
	s_and_saveexec_b64 s[40:41], s[4:5]
	s_cbranch_execz .LBB0_168
	v_lshl_add_u64 v[20:21], v[14:15], 0, v[16:17]
	v_add_co_u32_e32 v20, vcc, 0x8f000, v20
	s_nop 1
	v_addc_co_u32_e32 v21, vcc, 0, v21, vcc
	global_load_dword v87, v[20:21], off nt
.LBB0_168:
	s_or_b64 exec, exec, s[40:41]
	v_mov_b32_e32 v21, 0
	v_mov_b32_e32 v20, 0
	s_and_saveexec_b64 s[40:41], s[4:5]
	s_cbranch_execz .LBB0_170
	v_lshl_add_u64 v[22:23], v[14:15], 0, v[16:17]
	v_add_co_u32_e32 v22, vcc, 0x9a000, v22
	s_nop 1
	v_addc_co_u32_e32 v23, vcc, 0, v23, vcc
	global_load_dword v20, v[22:23], off nt
.LBB0_170:
	s_or_b64 exec, exec, s[40:41]
	s_and_saveexec_b64 s[40:41], s[4:5]
	s_cbranch_execz .LBB0_172
	v_lshl_add_u64 v[22:23], v[14:15], 0, v[16:17]
	v_add_co_u32_e32 v22, vcc, 0xa5000, v22
	s_nop 1
	v_addc_co_u32_e32 v23, vcc, 0, v23, vcc
	global_load_dword v21, v[22:23], off nt
.LBB0_172:
	s_or_b64 exec, exec, s[40:41]
	v_mov_b32_e32 v89, 0
	v_mov_b32_e32 v90, 0
	s_and_saveexec_b64 s[40:41], s[4:5]
	s_cbranch_execz .LBB0_174
	v_lshl_add_u64 v[22:23], v[14:15], 0, v[16:17]
	v_add_co_u32_e32 v22, vcc, 0xb0000, v22
	s_nop 1
	v_addc_co_u32_e32 v23, vcc, 0, v23, vcc
	global_load_dword v90, v[22:23], off nt
.LBB0_174:
	s_or_b64 exec, exec, s[40:41]
	s_and_saveexec_b64 s[40:41], s[4:5]
	s_cbranch_execz .LBB0_176
	v_lshl_add_u64 v[22:23], v[14:15], 0, v[16:17]
	v_add_co_u32_e32 v22, vcc, 0xbb000, v22
	s_nop 1
	v_addc_co_u32_e32 v23, vcc, 0, v23, vcc
	global_load_dword v89, v[22:23], off nt
.LBB0_176:
	s_or_b64 exec, exec, s[40:41]
	v_mov_b32_e32 v23, 0
	v_mov_b32_e32 v22, 0
	s_and_saveexec_b64 s[40:41], s[4:5]
	s_cbranch_execz .LBB0_178
	v_lshl_add_u64 v[24:25], v[14:15], 0, v[16:17]
	v_add_co_u32_e32 v24, vcc, 0xc6000, v24
	s_nop 1
	v_addc_co_u32_e32 v25, vcc, 0, v25, vcc
	global_load_dword v22, v[24:25], off nt
.LBB0_178:
	s_or_b64 exec, exec, s[40:41]
	s_and_saveexec_b64 s[40:41], s[4:5]
	s_cbranch_execz .LBB0_180
	v_lshl_add_u64 v[24:25], v[14:15], 0, v[16:17]
	v_add_co_u32_e32 v24, vcc, 0xd1000, v24
	s_nop 1
	v_addc_co_u32_e32 v25, vcc, 0, v25, vcc
	global_load_dword v23, v[24:25], off nt
.LBB0_180:
	s_or_b64 exec, exec, s[40:41]
	v_mov_b32_e32 v91, 0
	v_mov_b32_e32 v92, 0
	s_and_saveexec_b64 s[40:41], s[4:5]
	s_cbranch_execz .LBB0_182
	v_lshl_add_u64 v[24:25], v[14:15], 0, v[16:17]
	v_add_co_u32_e32 v24, vcc, 0xdc000, v24
	s_nop 1
	v_addc_co_u32_e32 v25, vcc, 0, v25, vcc
	global_load_dword v92, v[24:25], off nt
.LBB0_182:
	s_or_b64 exec, exec, s[40:41]
	s_and_saveexec_b64 s[40:41], s[4:5]
	s_cbranch_execz .LBB0_184
	v_lshl_add_u64 v[24:25], v[14:15], 0, v[16:17]
	v_add_co_u32_e32 v24, vcc, 0xe7000, v24
	s_nop 1
	v_addc_co_u32_e32 v25, vcc, 0, v25, vcc
	global_load_dword v91, v[24:25], off nt
.LBB0_184:
	s_or_b64 exec, exec, s[40:41]
	v_mov_b32_e32 v25, 0
	v_mov_b32_e32 v24, 0
	s_and_saveexec_b64 s[40:41], s[4:5]
	s_cbranch_execz .LBB0_186
	v_lshl_add_u64 v[26:27], v[14:15], 0, v[16:17]
	v_add_co_u32_e32 v26, vcc, 0xf2000, v26
	s_nop 1
	v_addc_co_u32_e32 v27, vcc, 0, v27, vcc
	global_load_dword v24, v[26:27], off nt
.LBB0_186:
	s_or_b64 exec, exec, s[40:41]
	s_and_saveexec_b64 s[40:41], s[4:5]
	s_cbranch_execz .LBB0_188
	v_lshl_add_u64 v[26:27], v[14:15], 0, v[16:17]
	v_add_co_u32_e32 v26, vcc, 0xfd000, v26
	s_nop 1
	v_addc_co_u32_e32 v27, vcc, 0, v27, vcc
	global_load_dword v25, v[26:27], off nt
.LBB0_188:
	s_or_b64 exec, exec, s[40:41]
	v_mov_b32_e32 v93, 0
	v_mov_b32_e32 v94, 0
	s_and_saveexec_b64 s[40:41], s[4:5]
	s_cbranch_execz .LBB0_190
	v_lshl_add_u64 v[26:27], v[14:15], 0, v[16:17]
	v_add_co_u32_e32 v26, vcc, 0x108000, v26
	s_nop 1
	v_addc_co_u32_e32 v27, vcc, 0, v27, vcc
	global_load_dword v94, v[26:27], off nt
.LBB0_190:
	s_or_b64 exec, exec, s[40:41]
	s_and_saveexec_b64 s[40:41], s[4:5]
	s_cbranch_execz .LBB0_192
	v_lshl_add_u64 v[26:27], v[14:15], 0, v[16:17]
	v_add_co_u32_e32 v26, vcc, 0x113000, v26
	s_nop 1
	v_addc_co_u32_e32 v27, vcc, 0, v27, vcc
	global_load_dword v93, v[26:27], off nt
.LBB0_192:
	s_or_b64 exec, exec, s[40:41]
	v_mov_b32_e32 v27, 0
	v_mov_b32_e32 v26, 0
	s_and_saveexec_b64 s[40:41], s[4:5]
	s_cbranch_execz .LBB0_194
	v_lshl_add_u64 v[28:29], v[14:15], 0, v[16:17]
	v_add_co_u32_e32 v28, vcc, 0x11e000, v28
	s_nop 1
	v_addc_co_u32_e32 v29, vcc, 0, v29, vcc
	global_load_dword v26, v[28:29], off nt
.LBB0_194:
	s_or_b64 exec, exec, s[40:41]
	s_and_saveexec_b64 s[40:41], s[4:5]
	s_cbranch_execz .LBB0_196
	v_lshl_add_u64 v[28:29], v[14:15], 0, v[16:17]
	v_add_co_u32_e32 v28, vcc, 0x129000, v28
	s_nop 1
	v_addc_co_u32_e32 v29, vcc, 0, v29, vcc
	global_load_dword v27, v[28:29], off nt
.LBB0_196:
	s_or_b64 exec, exec, s[40:41]
	v_mov_b32_e32 v95, 0
	v_mov_b32_e32 v96, 0
	s_and_saveexec_b64 s[40:41], s[4:5]
	s_cbranch_execz .LBB0_198
	v_lshl_add_u64 v[28:29], v[14:15], 0, v[16:17]
	v_add_co_u32_e32 v28, vcc, 0x134000, v28
	s_nop 1
	v_addc_co_u32_e32 v29, vcc, 0, v29, vcc
	global_load_dword v96, v[28:29], off nt
.LBB0_198:
	s_or_b64 exec, exec, s[40:41]
	s_and_saveexec_b64 s[40:41], s[4:5]
	s_cbranch_execz .LBB0_200
	v_lshl_add_u64 v[28:29], v[14:15], 0, v[16:17]
	v_add_co_u32_e32 v28, vcc, 0x13f000, v28
	s_nop 1
	v_addc_co_u32_e32 v29, vcc, 0, v29, vcc
	global_load_dword v95, v[28:29], off nt
.LBB0_200:
	s_or_b64 exec, exec, s[40:41]
	v_mov_b32_e32 v29, 0
	v_mov_b32_e32 v28, 0
	s_and_saveexec_b64 s[40:41], s[4:5]
	s_cbranch_execz .LBB0_202
	v_lshl_add_u64 v[98:99], v[14:15], 0, v[16:17]
	v_add_co_u32_e32 v98, vcc, 0x14a000, v98
	s_nop 1
	v_addc_co_u32_e32 v99, vcc, 0, v99, vcc
	global_load_dword v28, v[98:99], off nt
.LBB0_202:
	s_or_b64 exec, exec, s[40:41]
	s_and_saveexec_b64 s[40:41], s[4:5]
	s_cbranch_execz .LBB0_204
	v_lshl_add_u64 v[14:15], v[14:15], 0, v[16:17]
	v_add_co_u32_e32 v14, vcc, 0x155000, v14
	s_nop 1
	v_addc_co_u32_e32 v15, vcc, 0, v15, vcc
	global_load_dword v29, v[14:15], off nt
.LBB0_204:
	s_or_b64 exec, exec, s[40:41]
	s_lshr_b32 s4, s89, 1
	s_lshl_b32 s5, s89, 1
	s_mul_i32 s4, s4, 3
	s_and_b32 s5, s5, 2
	s_add_i32 s4, s4, s5
	s_lshl_b32 s4, s4, 10
	s_ashr_i32 s5, s4, 31
	s_lshl_b64 s[4:5], s[4:5], 2
	s_add_u32 s40, s26, s4
	v_cndmask_b32_e64 v11, 0, 1, s[36:37]
	s_addc_u32 s41, s27, s5
	v_cmp_ne_u32_e64 s[4:5], 1, v11
	s_andn2_b64 vcc, exec, s[36:37]
	v_add_u32_e32 v14, v61, v70
	s_cbranch_vccnz .LBB0_227
	v_ashrrev_i32_e32 v11, 31, v10
	s_ashr_i32 s39, s38, 31
	v_lshl_add_u64 v[10:11], v[10:11], 2, s[40:41]
	v_lshl_add_u64 v[16:17], s[38:39], 0, v[2:3]
	v_lshl_add_u64 v[16:17], v[16:17], 2, s[40:41]
	global_load_dword v15, v[10:11], off nt
	global_load_dword v97, v[16:17], off offset:8 nt
	s_nop 0
	global_load_dword v10, v[16:17], off offset:16 nt
	global_load_dword v11, v[16:17], off offset:24 nt
	s_waitcnt vmcnt(3)
	v_mul_f32_e32 v15, v6, v15
	s_waitcnt vmcnt(2)
	v_mul_f32_e32 v16, v82, v97
	ds_write_b32 v62, v15
	s_waitcnt vmcnt(0)
	v_pk_mul_f32 v[10:11], v[8:9], v[10:11]
	ds_write_b32 v14, v16
	s_cbranch_execnz .LBB0_207

.LBB0_207:
	s_and_b64 vcc, exec, s[4:5]
	ds_write2_b32 v73, v10, v11 offset1:66
	s_cbranch_vccnz .LBB0_228
	s_ashr_i32 s39, s38, 31
	s_waitcnt vmcnt(0)
	v_lshl_add_u64 v[8:9], s[38:39], 0, v[2:3]
	v_lshl_add_u64 v[8:9], v[8:9], 2, s[40:41]
	global_load_dword v6, v[8:9], off offset:32 nt
	global_load_dword v14, v[8:9], off offset:40 nt
	global_load_dword v10, v[8:9], off offset:48 nt
	global_load_dword v11, v[8:9], off offset:56 nt
	s_waitcnt vmcnt(3)
	v_mul_f32_e32 v6, v84, v6
	s_waitcnt vmcnt(2)
	v_mul_f32_e32 v14, v83, v14
	ds_write2_b32 v78, v6, v14 offset1:66
	s_waitcnt vmcnt(0)
	v_pk_mul_f32 v[8:9], v[12:13], v[10:11]
	s_cbranch_execnz .LBB0_210

.LBB0_210:
	s_and_b64 vcc, exec, s[4:5]
	s_waitcnt vmcnt(0)
	ds_write2_b32 v74, v8, v9 offset1:66
	s_cbranch_vccnz .LBB0_229
	s_ashr_i32 s39, s38, 31
	v_lshl_add_u64 v[8:9], s[38:39], 0, v[2:3]
	v_lshl_add_u64 v[8:9], v[8:9], 2, s[40:41]
	global_load_dword v6, v[8:9], off offset:64 nt
	global_load_dword v12, v[8:9], off offset:72 nt
	global_load_dword v10, v[8:9], off offset:80 nt
	global_load_dword v11, v[8:9], off offset:88 nt
	s_waitcnt vmcnt(3)
	v_mul_f32_e32 v6, v86, v6
	s_waitcnt vmcnt(2)
	v_mul_f32_e32 v12, v85, v12
	ds_write2_b32 v79, v6, v12 offset1:66
	s_waitcnt vmcnt(0)
	v_pk_mul_f32 v[8:9], v[18:19], v[10:11]
	s_cbranch_execnz .LBB0_213

.LBB0_213:
	s_and_b64 vcc, exec, s[4:5]
	ds_write2_b32 v75, v8, v9 offset1:66
	s_cbranch_vccnz .LBB0_230
	s_ashr_i32 s39, s38, 31
	v_lshl_add_u64 v[8:9], s[38:39], 0, v[2:3]
	v_lshl_add_u64 v[8:9], v[8:9], 2, s[40:41]
	global_load_dword v6, v[8:9], off offset:96 nt
	global_load_dword v12, v[8:9], off offset:104 nt
	global_load_dword v10, v[8:9], off offset:112 nt
	global_load_dword v11, v[8:9], off offset:120 nt
	s_waitcnt vmcnt(3)
	v_mul_f32_e32 v6, v88, v6
	s_waitcnt vmcnt(2)
	v_mul_f32_e32 v12, v87, v12
	ds_write2_b32 v80, v6, v12 offset1:66
	s_waitcnt vmcnt(0)
	v_pk_mul_f32 v[8:9], v[20:21], v[10:11]
	s_cbranch_execnz .LBB0_216

.LBB0_216:
	v_add_u32_e32 v6, v61, v71
	s_and_b64 vcc, exec, s[4:5]
	v_add_u32_e32 v10, 0x200, v6
	ds_write2_b32 v6, v8, v9 offset0:66 offset1:132
	s_cbranch_vccnz .LBB0_231
	s_ashr_i32 s39, s38, 31
	v_lshl_add_u64 v[8:9], s[38:39], 0, v[2:3]
	v_lshl_add_u64 v[8:9], v[8:9], 2, s[40:41]
	global_load_dword v11, v[8:9], off offset:128 nt
	global_load_dword v14, v[8:9], off offset:136 nt
	global_load_dword v12, v[8:9], off offset:144 nt
	global_load_dword v13, v[8:9], off offset:152 nt
	s_waitcnt vmcnt(3)
	v_mul_f32_e32 v11, v90, v11
	s_waitcnt vmcnt(2)
	v_mul_f32_e32 v14, v89, v14
	ds_write2_b32 v10, v11, v14 offset0:70 offset1:136
	s_waitcnt vmcnt(0)
	v_pk_mul_f32 v[8:9], v[22:23], v[12:13]
	s_cbranch_execnz .LBB0_219

.LBB0_219:
	v_add_u32_e32 v10, 0x400, v6
	ds_write2_b32 v10, v8, v9 offset0:74 offset1:140
	s_and_b64 vcc, exec, s[4:5]
	v_add_u32_e32 v10, 0x600, v6
	s_cbranch_vccnz .LBB0_232
	s_ashr_i32 s39, s38, 31
	v_lshl_add_u64 v[8:9], s[38:39], 0, v[2:3]
	v_lshl_add_u64 v[8:9], v[8:9], 2, s[40:41]
	global_load_dword v11, v[8:9], off offset:160 nt
	global_load_dword v14, v[8:9], off offset:168 nt
	global_load_dword v12, v[8:9], off offset:176 nt
	global_load_dword v13, v[8:9], off offset:184 nt
	s_waitcnt vmcnt(3)
	v_mul_f32_e32 v11, v92, v11
	s_waitcnt vmcnt(2)
	v_mul_f32_e32 v14, v91, v14
	ds_write2_b32 v10, v11, v14 offset0:78 offset1:144
	s_waitcnt vmcnt(0)
	v_pk_mul_f32 v[8:9], v[24:25], v[12:13]
	s_cbranch_execnz .LBB0_222

.LBB0_222:
	v_add_u32_e32 v10, 0x800, v6
	ds_write2_b32 v10, v8, v9 offset0:82 offset1:148
	s_and_b64 vcc, exec, s[4:5]
	v_add_u32_e32 v10, 0xa00, v6
	s_cbranch_vccnz .LBB0_233
	s_ashr_i32 s39, s38, 31
	v_lshl_add_u64 v[8:9], s[38:39], 0, v[2:3]
	v_lshl_add_u64 v[8:9], v[8:9], 2, s[40:41]
	global_load_dword v11, v[8:9], off offset:192 nt
	global_load_dword v14, v[8:9], off offset:200 nt
	global_load_dword v12, v[8:9], off offset:208 nt
	global_load_dword v13, v[8:9], off offset:216 nt
	s_waitcnt vmcnt(3)
	v_mul_f32_e32 v11, v94, v11
	s_waitcnt vmcnt(2)
	v_mul_f32_e32 v14, v93, v14
	ds_write2_b32 v10, v11, v14 offset0:86 offset1:152
	s_waitcnt vmcnt(0)
	v_pk_mul_f32 v[8:9], v[26:27], v[12:13]
	s_cbranch_execnz .LBB0_225

.LBB0_225:
	v_add_u32_e32 v10, 0xc00, v6
	ds_write2_b32 v10, v8, v9 offset0:90 offset1:156
	s_and_b64 vcc, exec, s[4:5]
	v_add_u32_e32 v10, 0xe00, v6
	s_cbranch_vccnz .LBB0_234
	s_ashr_i32 s39, s38, 31
	v_lshl_add_u64 v[8:9], s[38:39], 0, v[2:3]
	v_lshl_add_u64 v[8:9], v[8:9], 2, s[40:41]
	global_load_dword v11, v[8:9], off offset:224 nt
	global_load_dword v14, v[8:9], off offset:232 nt
	global_load_dword v12, v[8:9], off offset:240 nt
	global_load_dword v13, v[8:9], off offset:248 nt
	s_waitcnt vmcnt(3)
	v_mul_f32_e32 v11, v96, v11
	s_waitcnt vmcnt(2)
	v_mul_f32_e32 v14, v95, v14
	ds_write2_b32 v10, v11, v14 offset0:94 offset1:160
	s_waitcnt vmcnt(0)
	v_pk_mul_f32 v[8:9], v[28:29], v[12:13]
	s_cbranch_execnz .LBB0_17
	s_branch .LBB0_16

.LBB0_238:
	s_ashr_i32 s19, s18, 31
	s_lshl_b64 s[16:17], s[18:19], 12
	v_lshl_add_u64 v[46:47], v[34:35], 0, s[16:17]
	global_load_dwordx4 v[30:33], v[46:47], off nt
	global_load_dwordx4 v[26:29], v[46:47], off offset:1024 nt
	global_load_dwordx4 v[18:21], v[46:47], off offset:2048 nt
	global_load_dwordx4 v[22:25], v[46:47], off offset:3072 nt
	s_add_i32 s16, s18, s46
	s_cmp_lt_i32 s16, 0x8000
	s_cselect_b64 s[22:23], -1, 0
	s_cmpk_gt_i32 s16, 0x7fff
	s_cbranch_scc1 .LBB0_240
	s_ashr_i32 s17, s16, 31
	s_lshl_b64 s[24:25], s[16:17], 12
	v_lshl_add_u64 v[46:47], v[34:35], 0, s[24:25]
	global_load_dwordx4 v[14:17], v[46:47], off nt
	global_load_dwordx4 v[10:13], v[46:47], off offset:1024 nt
	global_load_dwordx4 v[6:9], v[46:47], off offset:2048 nt
	global_load_dwordx4 v[2:5], v[46:47], off offset:3072 nt

.LBB0_249:
	v_ashrrev_i32_e32 v7, 6, v6
	v_lshrrev_b32_e32 v10, 2, v6
	v_mul_hi_i32 v11, v7, s18
	v_mul_hi_i32 v12, v7, s23
	v_and_b32_e32 v13, 8, v10
	v_lshrrev_b32_e32 v10, 31, v11
	v_lshrrev_b32_e32 v14, 4, v12
	v_lshrrev_b32_e32 v15, 31, v12
	v_lshrrev_b32_e32 v12, 6, v12
	v_add_u32_e32 v16, v11, v10
	v_add_u32_e32 v10, v14, v15
	v_add_u32_e32 v14, v12, v15
	v_lshl_add_u32 v11, v16, 1, v16
	v_mul_hi_i32 v12, v16, s19
	v_sub_u32_e32 v7, v7, v11
	v_lshrrev_b32_e32 v17, 31, v12
	v_lshrrev_b32_e32 v12, 2, v12
	v_and_b32_e32 v15, 3, v10
	v_add_u32_e32 v12, v12, v17
	v_lshlrev_b32_e32 v7, 5, v7
	v_mul_lo_u32 v12, v12, 24
	v_mad_u32_u24 v7, v15, s24, v7
	v_mul_i32_i24_e32 v10, 0x180, v14
	v_sub_u32_e32 v15, v16, v12
	v_or_b32_e32 v12, v7, v40
	v_mad_i64_i32 v[10:11], s[30:31], v10, s26, v[4:5]
	v_lshl_or_b32 v7, v15, 4, v13
	v_ashrrev_i32_e32 v13, 31, v12
	v_lshl_add_u64 v[10:11], v[12:13], 2, v[10:11]
	v_mad_i32_i24 v12, v14, s25, v7
	v_mul_i32_i24_e32 v14, 0x180, v7
	v_ashrrev_i32_e32 v15, 31, v14
	v_ashrrev_i32_e32 v13, 31, v12
	v_lshl_add_u64 v[18:19], v[14:15], 2, v[10:11]
	v_lshl_add_u64 v[20:21], v[12:13], 2, s[8:9]
	global_load_dwordx4 v[10:13], v[20:21], off offset:16 nt
	global_load_dwordx4 v[14:17], v[20:21], off nt
	global_load_dword v22, v[18:19], off nt
	global_load_dword v23, v[18:19], off offset:1536 nt
	global_load_dword v24, v[18:19], off offset:3072 nt
	v_add_co_u32_e32 v20, vcc, s10, v18
	v_add_u32_e32 v6, s22, v6
	s_nop 0
	v_addc_co_u32_e32 v21, vcc, 0, v19, vcc
	v_add_co_u32_e32 v18, vcc, s11, v18
	s_waitcnt vmcnt(1)
	v_pk_mul_f32 v[14:15], v[22:23], v[14:15]
	v_addc_co_u32_e32 v19, vcc, 0, v19, vcc
	global_load_dword v25, v[20:21], off offset:512 nt
	global_load_dword v26, v[20:21], off offset:2048 nt
	global_load_dword v27, v[20:21], off offset:3584 nt
	global_load_dword v28, v[18:19], off offset:1024 nt
	global_load_dword v29, v[18:19], off offset:2560 nt
	v_cmp_lt_i32_e32 vcc, s27, v6
	s_or_b64 s[16:17], vcc, s[16:17]
	s_waitcnt vmcnt(4)
	v_pk_mul_f32 v[16:17], v[24:25], v[16:17]
	s_waitcnt vmcnt(2)
	v_pk_mul_f32 v[18:19], v[26:27], v[10:11]
	v_cvt_pk_bf16_f32 v10, v14, v15
	s_waitcnt vmcnt(0)
	v_pk_mul_f32 v[20:21], v[28:29], v[12:13]
	v_cvt_pk_bf16_f32 v11, v16, v17
	v_cvt_pk_bf16_f32 v12, v18, v19
	v_cvt_pk_bf16_f32 v13, v20, v21
	global_store_dwordx4 v[2:3], v[10:13], off
	v_lshl_add_u64 v[2:3], v[2:3], 0, s[6:7]
	s_andn2_b64 exec, exec, s[16:17]
	s_cbranch_execnz .LBB0_249

.LBB0_252:
	v_ashrrev_i32_e32 v10, 14, v6
	v_lshrrev_b32_e32 v4, 5, v6
	v_lshrrev_b32_e32 v7, 1, v6
	v_lshrrev_b32_e32 v11, 2, v6
	v_lshrrev_b32_e32 v12, 4, v6
	v_and_b32_e32 v4, 0x180, v4
	v_and_b32_e32 v7, 0x60, v7
	v_and_b32_e32 v13, 8, v11
	v_ashrrev_i32_e32 v11, 31, v10
	v_or3_b32 v4, v7, v40, v4
	v_and_or_b32 v7, v12, s16, v13
	v_lshlrev_b64 v[12:13], 19, v[10:11]
	v_lshl_add_u64 v[12:13], s[14:15], 0, v[12:13]
	v_lshlrev_b32_e32 v4, 2, v4
	v_lshl_or_b32 v10, v10, 8, v7
	v_lshl_add_u64 v[12:13], v[12:13], 0, v[4:5]
	v_lshlrev_b32_e32 v4, 11, v7
	v_ashrrev_i32_e32 v11, 31, v10
	v_lshl_add_u64 v[18:19], v[12:13], 0, v[4:5]
	v_lshl_add_u64 v[20:21], v[10:11], 2, s[12:13]
	global_load_dword v22, v[18:19], off nt
	global_load_dword v23, v[18:19], off offset:2048 nt
	global_load_dwordx4 v[10:13], v[20:21], off offset:16 nt
	global_load_dwordx4 v[14:17], v[20:21], off nt
	v_add_co_u32_e32 v20, vcc, s17, v18
	v_add_u32_e32 v6, s22, v6
	s_nop 0
	v_addc_co_u32_e32 v21, vcc, 0, v19, vcc
	v_add_co_u32_e32 v24, vcc, s18, v18
	s_waitcnt vmcnt(0)
	v_pk_mul_f32 v[14:15], v[22:23], v[14:15]
	v_addc_co_u32_e32 v25, vcc, 0, v19, vcc
	v_add_co_u32_e32 v18, vcc, s19, v18
	s_nop 1
	v_addc_co_u32_e32 v19, vcc, 0, v19, vcc
	global_load_dword v26, v[24:25], off offset:-4096 nt
	global_load_dword v27, v[20:21], off offset:2048 nt
	global_load_dword v28, v[24:25], off nt
	global_load_dword v29, v[24:25], off offset:2048 nt
	global_load_dword v30, v[18:19], off nt
	global_load_dword v31, v[18:19], off offset:2048 nt
	v_cmp_lt_i32_e32 vcc, s23, v6
	s_or_b64 s[10:11], vcc, s[10:11]
	s_waitcnt vmcnt(4)
	v_pk_mul_f32 v[16:17], v[26:27], v[16:17]
	s_waitcnt vmcnt(2)
	v_pk_mul_f32 v[18:19], v[28:29], v[10:11]
	v_cvt_pk_bf16_f32 v10, v14, v15
	s_waitcnt vmcnt(0)
	v_pk_mul_f32 v[20:21], v[30:31], v[12:13]
	v_cvt_pk_bf16_f32 v11, v16, v17
	v_cvt_pk_bf16_f32 v12, v18, v19
	v_cvt_pk_bf16_f32 v13, v20, v21
	global_store_dwordx4 v[2:3], v[10:13], off
	v_lshl_add_u64 v[2:3], v[2:3], 0, s[8:9]
	s_andn2_b64 exec, exec, s[10:11]
	s_cbranch_execnz .LBB0_252

.LBB0_255:
	s_or_b64 exec, exec, s[14:15]
	v_lshl_add_u32 v6, v3, 5, v5
	v_ashrrev_i32_e32 v7, 31, v6
	v_lshl_add_u64 v[6:7], v[6:7], 2, s[20:21]
	global_load_dword v3, v[6:7], off nt
	s_waitcnt vmcnt(0)
	v_mul_f32_e32 v5, 0x3fb8aa3b, v3

.LBB0_262:
	s_or_b64 exec, exec, s[14:15]
	v_lshlrev_b32_e32 v10, 5, v3
	v_ashrrev_i32_e32 v5, 31, v4
	v_ashrrev_i32_e32 v11, 31, v10
	v_lshl_add_u64 v[4:5], v[10:11], 0, v[4:5]
	v_lshl_add_u64 v[4:5], v[4:5], 2, s[20:21]
	global_load_dword v3, v[4:5], off offset:1024 nt
	s_waitcnt vmcnt(0)
	v_mul_f32_e32 v5, 0x3fb8aa3b, v3
